# speedup vs baseline: 1.0155x; 1.0031x over previous
_Z8gemm_bigIN3pg85EpiUPEEvNS0_4GemmET_:
	s_mov_b32 s44, 0x3dd2d3e8
	s_mov_b32 s45, 0x3dd2d3e8
	s_mov_b32 s46, 0xc0135761
	s_mov_b32 s47, 0xc0135761
	s_mov_b32 s48, 1.0
	s_mov_b32 s49, 1.0
	v_lshlrev_b32_e32 v1, 4, v0
	v_and_b32_e32 v2, 32, v0
	v_bitop3_b32 v129, v1, v2, 48 bitop3:0x6c
	v_and_b32_e32 v138, 64, v0
	v_or_b32_e32 v1, v129, v138
	s_load_dwordx4 s[8:11], s[0:1], 0x0
	s_load_dword s16, s[0:1], 0x18
	v_lshrrev_b32_e32 v2, 1, v1
	v_lshrrev_b32_e32 v1, 1, v0
	v_and_b32_e32 v140, 24, v1
	v_lshrrev_b32_e32 v1, 5, v0
	v_and_b32_e32 v1, 4, v1
	v_bfe_u32 v3, v0, 2, 2
	v_or3_b32 v3, v1, v3, v140
	v_lshrrev_b32_e32 v4, 3, v0
	v_bfe_u32 v139, v0, 2, 4
	v_and_b32_e32 v1, 48, v4
	v_and_or_b32 v4, v4, 32, v3
	v_or_b32_e32 v5, v1, v139
	s_waitcnt lgkmcnt(0)
	v_mul_lo_u32 v4, s16, v4
	s_lshl_b32 s3, s2, 2
	s_bfe_u32 s31, s2, 0x20003
	s_ashr_i32 s18, s2, 5
	v_mul_lo_u32 v5, s16, v5
	v_add_lshl_u32 v130, v4, v2, 1
	v_bfe_u32 v4, v0, 3, 25
	s_movk_i32 s2, 0x70
	s_and_b32 s30, s3, 28
	v_add_lshl_u32 v132, v5, v2, 1
	v_or_b32_e32 v5, 64, v4
	v_bitop3_b32 v142, v4, s2, 64 bitop3:0xc8
	s_movk_i32 s2, 0x60
	s_ashr_i32 s17, s16, 31
	s_or_b32 s19, s30, s31
	v_and_or_b32 v3, v5, s2, v3
	s_lshl_b32 s4, s16, 9
	s_lshr_b64 s[2:3], s[16:17], 23
	s_mul_hi_u32 s5, s4, s19
	s_mul_i32 s3, s2, s19
	s_add_i32 s5, s5, s3
	s_ashr_i32 s3, s18, 31
	v_readfirstlane_b32 s20, v0
	s_mul_hi_u32 s7, s4, s18
	s_mul_i32 s3, s4, s3
	s_lshr_b32 s14, s20, 6
	s_add_i32 s3, s7, s3
	s_mul_i32 s2, s2, s18
	s_lshr_b32 s33, s20, 8
	s_lshl_b32 s39, s14, 10
	s_mul_i32 s6, s4, s19
	s_add_i32 s3, s3, s2
	s_mul_i32 s4, s4, s18
	s_add_u32 s2, s10, s4
	s_addc_u32 s3, s11, s3
	s_add_i32 s22, s39, 0
	s_add_i32 m0, s22, 0x10000
	v_mul_lo_u32 v3, s16, v3
	global_load_lds_dwordx4 v130, s[2:3]
	s_add_i32 m0, s22, 0x12000
	s_lshl_b64 s[10:11], s[16:17], 8
	v_add_lshl_u32 v136, v3, v2, 1
	s_add_u32 s26, s2, s10
	global_load_lds_dwordx4 v136, s[2:3]
	s_addc_u32 s27, s3, s11
	s_add_i32 m0, s22, 0x14000
	v_or_b32_e32 v4, v142, v139
	global_load_lds_dwordx4 v130, s[26:27]
	s_add_i32 m0, s22, 0x16000
	s_add_u32 s12, s8, s6
	s_addc_u32 s13, s9, s5
	s_add_i32 s23, s22, 0x2000
	v_mul_lo_u32 v4, s16, v4
	global_load_lds_dwordx4 v136, s[26:27]
	s_mov_b32 m0, s22
	s_add_u32 s4, s12, s10
	v_add_lshl_u32 v134, v4, v2, 1
	global_load_lds_dwordx4 v132, s[12:13]
	s_mov_b32 m0, s23
	s_addc_u32 s5, s13, s11
	s_add_i32 s24, s22, 0x4000
	global_load_lds_dwordx4 v134, s[12:13]
	s_mov_b32 m0, s24
	s_add_i32 s25, s22, 0x6000
	global_load_lds_dwordx4 v132, s[4:5]
	s_mov_b32 m0, s25
	v_mov_b32_e32 v131, 0
	global_load_lds_dwordx4 v134, s[4:5]
	s_load_dwordx4 s[4:7], s[0:1], 0x30
	v_mov_b32_e32 v137, v131
	v_mov_b32_e32 v133, v131
	v_mov_b32_e32 v135, v131
	v_lshl_add_u64 v[12:13], s[2:3], 0, v[130:131]
	v_lshl_add_u64 v[8:9], s[2:3], 0, v[136:137]
	v_lshl_add_u64 v[4:5], s[26:27], 0, v[130:131]
	v_lshl_add_u64 v[2:3], s[26:27], 0, v[136:137]
	v_lshl_add_u64 v[10:11], s[12:13], 0, v[132:133]
	s_cmp_lg_u32 s33, 1
	v_lshl_add_u64 v[6:7], s[12:13], 0, v[134:135]
	s_cbranch_scc1 .LBB6_2
	s_barrier

.LBB6_8:
	s_lshl_b32 s0, s19, 8
	s_add_i32 s21, s21, s0
	v_or_b32_e32 v0, s21, v141
	v_mov_b32_e32 v1, 0
	v_lshlrev_b64 v[132:133], 6, v[0:1]
	s_waitcnt lgkmcnt(0)
	v_lshl_add_u64 v[132:133], s[10:11], 0, v[132:133]
	s_barrier
	global_load_dwordx4 v[134:137], v[132:133], off
	global_load_dwordx4 v[142:145], v[132:133], off offset:32
	global_load_dwordx4 v[146:149], v[132:133], off offset:16
	global_load_dwordx4 v[150:153], v[132:133], off offset:48
	s_lshl_b32 s1, s18, 8
	s_or_b32 s1, s7, s1
	v_or_b32_e32 v130, s1, v140
	v_mov_b32_e32 v132, s5
	v_mov_b32_e32 v129, v131
	s_mov_b32 s0, 0xc0135761
	v_mad_i64_i32 v[138:139], s[2:3], v0, s4, 0
	v_ashrrev_i32_e32 v131, 31, v130
	v_lshlrev_b64 v[130:131], 1, v[130:131]
	s_waitcnt vmcnt(0)
	v_mov_b32_e32 v140, v134
	v_mov_b32_e32 v141, v142
	v_mov_b32_e32 v142, v135
	v_mov_b32_e32 v134, v136
	v_mov_b32_e32 v135, v144
	v_mov_b32_e32 v144, v137
	v_mov_b32_e32 v136, v146
	v_mov_b32_e32 v137, v150
	v_mov_b32_e32 v150, v147
	v_mov_b32_e32 v146, v148
	v_mov_b32_e32 v147, v152
	v_mov_b32_e32 v152, v149
	v_pk_add_f32 v[140:141], v[140:141], v[142:143]
	v_pk_add_f32 v[134:135], v[134:135], v[144:145]
	v_pk_add_f32 v[136:137], v[136:137], v[150:151]
	v_pk_add_f32 v[142:143], v[146:147], v[152:153]
	v_pk_add_f32 v[134:135], v[140:141], v[134:135]
	v_pk_add_f32 v[136:137], v[136:137], v[142:143]
	s_nop 0
	v_pk_add_f32 v[134:135], v[134:135], v[136:137]
	v_lshl_add_u64 v[136:137], v[138:139], 1, s[8:9]
	v_add_f32_e32 v133, v134, v135
	v_fma_f32 v133, s6, v133, v132
	v_rsq_f32_e32 v134, v133
	v_lshl_add_u64 v[136:137], v[136:137], 0, v[130:131]
	v_pk_mul_f32 v[126:127], v[126:127], v[134:135] op_sel_hi:[1,0]
	v_pk_mul_f32 v[128:129], v[128:129], v[134:135] op_sel_hi:[1,0]
	v_pk_mul_f32 v[122:123], v[122:123], v[134:135] op_sel_hi:[1,0]
	v_pk_mul_f32 v[124:125], v[124:125], v[134:135] op_sel_hi:[1,0]
	v_pk_mul_f32 v[118:119], v[118:119], v[134:135] op_sel_hi:[1,0]
	v_pk_mul_f32 v[120:121], v[120:121], v[134:135] op_sel_hi:[1,0]
	v_pk_mul_f32 v[114:115], v[114:115], v[134:135] op_sel_hi:[1,0]
	v_pk_mul_f32 v[116:117], v[116:117], v[134:135] op_sel_hi:[1,0]
	v_pk_mul_f32 v[138:139], v[126:127], s[44:45]
	v_pk_mul_f32 v[140:141], v[128:129], s[44:45]
	v_pk_mul_f32 v[142:143], v[122:123], s[44:45]
	v_pk_mul_f32 v[144:145], v[124:125], s[44:45]
	v_pk_fma_f32 v[138:139], v[126:127], v[138:139], s[46:47] neg_lo:[1,0,0] neg_hi:[1,0,0]
	v_pk_fma_f32 v[140:141], v[128:129], v[140:141], s[46:47] neg_lo:[1,0,0] neg_hi:[1,0,0]
	v_pk_fma_f32 v[142:143], v[122:123], v[142:143], s[46:47] neg_lo:[1,0,0] neg_hi:[1,0,0]
	v_pk_fma_f32 v[144:145], v[124:125], v[144:145], s[46:47] neg_lo:[1,0,0] neg_hi:[1,0,0]
	v_pk_mul_f32 v[138:139], v[126:127], v[138:139]
	v_pk_mul_f32 v[140:141], v[128:129], v[140:141]
	v_pk_mul_f32 v[142:143], v[122:123], v[142:143]
	v_pk_mul_f32 v[144:145], v[124:125], v[144:145]
	v_exp_f32_e32 v138, v138
	v_exp_f32_e32 v139, v139
	v_exp_f32_e32 v140, v140
	v_exp_f32_e32 v141, v141
	v_exp_f32_e32 v142, v142
	v_exp_f32_e32 v143, v143
	v_exp_f32_e32 v144, v144
	v_exp_f32_e32 v145, v145
	v_pk_add_f32 v[138:139], v[138:139], s[48:49]
	v_pk_add_f32 v[140:141], v[140:141], s[48:49]
	v_pk_add_f32 v[142:143], v[142:143], s[48:49]
	v_pk_add_f32 v[144:145], v[144:145], s[48:49]
	v_rcp_f32_e32 v138, v138
	v_rcp_f32_e32 v139, v139
	v_rcp_f32_e32 v140, v140
	v_rcp_f32_e32 v141, v141
	v_rcp_f32_e32 v142, v142
	v_rcp_f32_e32 v143, v143
	v_rcp_f32_e32 v144, v144
	v_rcp_f32_e32 v145, v145
	s_nop 0
	v_pk_mul_f32 v[126:127], v[126:127], v[138:139]
	v_pk_mul_f32 v[128:129], v[128:129], v[140:141]
	v_pk_mul_f32 v[122:123], v[122:123], v[142:143]
	v_pk_mul_f32 v[124:125], v[124:125], v[144:145]
	v_cvt_pk_bf16_f32 v138, v126, v127
	v_cvt_pk_bf16_f32 v139, v128, v129
	v_cvt_pk_bf16_f32 v140, v122, v123
	v_cvt_pk_bf16_f32 v141, v124, v125
	global_store_dwordx4 v[136:137], v[138:141], off
	v_pk_mul_f32 v[126:127], v[118:119], s[44:45]
	v_pk_mul_f32 v[128:129], v[120:121], s[44:45]
	v_pk_mul_f32 v[122:123], v[114:115], s[44:45]
	v_pk_mul_f32 v[124:125], v[116:117], s[44:45]
	v_pk_fma_f32 v[126:127], v[118:119], v[126:127], s[46:47] neg_lo:[1,0,0] neg_hi:[1,0,0]
	v_pk_fma_f32 v[128:129], v[120:121], v[128:129], s[46:47] neg_lo:[1,0,0] neg_hi:[1,0,0]
	v_pk_fma_f32 v[122:123], v[114:115], v[122:123], s[46:47] neg_lo:[1,0,0] neg_hi:[1,0,0]
	v_pk_fma_f32 v[124:125], v[116:117], v[124:125], s[46:47] neg_lo:[1,0,0] neg_hi:[1,0,0]
	v_pk_mul_f32 v[126:127], v[118:119], v[126:127]
	v_pk_mul_f32 v[128:129], v[120:121], v[128:129]
	v_pk_mul_f32 v[122:123], v[114:115], v[122:123]
	v_pk_mul_f32 v[124:125], v[116:117], v[124:125]
	v_exp_f32_e32 v126, v126
	v_exp_f32_e32 v127, v127
	v_exp_f32_e32 v128, v128
	v_exp_f32_e32 v129, v129
	v_exp_f32_e32 v122, v122
	v_exp_f32_e32 v123, v123
	v_exp_f32_e32 v124, v124
	v_exp_f32_e32 v125, v125
	v_pk_add_f32 v[126:127], v[126:127], s[48:49]
	v_pk_add_f32 v[128:129], v[128:129], s[48:49]
	v_pk_add_f32 v[122:123], v[122:123], s[48:49]
	v_pk_add_f32 v[124:125], v[124:125], s[48:49]
	v_rcp_f32_e32 v126, v126
	v_rcp_f32_e32 v127, v127
	v_rcp_f32_e32 v128, v128
	v_rcp_f32_e32 v129, v129
	v_rcp_f32_e32 v122, v122
	v_rcp_f32_e32 v123, v123
	v_rcp_f32_e32 v124, v124
	v_rcp_f32_e32 v125, v125
	s_nop 0
	v_pk_mul_f32 v[118:119], v[118:119], v[126:127]
	v_pk_mul_f32 v[120:121], v[120:121], v[128:129]
	v_pk_mul_f32 v[114:115], v[114:115], v[122:123]
	v_pk_mul_f32 v[116:117], v[116:117], v[124:125]
	v_cvt_pk_bf16_f32 v142, v118, v119
	v_cvt_pk_bf16_f32 v143, v120, v121
	v_cvt_pk_bf16_f32 v144, v114, v115
	v_cvt_pk_bf16_f32 v145, v116, v117
	v_or_b32_e32 v134, 16, v0
	v_mov_b32_e32 v135, v1
	global_store_dwordx4 v[136:137], v[142:145], off offset:256
	s_nop 1
	v_lshlrev_b64 v[114:115], 6, v[134:135]
	v_lshl_add_u64 v[126:127], s[10:11], 0, v[114:115]
	global_load_dwordx4 v[114:117], v[126:127], off
	global_load_dwordx4 v[118:121], v[126:127], off offset:32
	global_load_dwordx4 v[122:125], v[126:127], off offset:16
	s_nop 0
	global_load_dwordx4 v[126:129], v[126:127], off offset:48
	s_waitcnt vmcnt(3)
	v_mov_b32_e32 v136, v114
	s_waitcnt vmcnt(2)
	v_mov_b32_e32 v137, v118
	v_mov_b32_e32 v118, v115
	v_mov_b32_e32 v114, v116
	v_mov_b32_e32 v115, v120
	v_mov_b32_e32 v120, v117
	s_waitcnt vmcnt(1)
	v_mov_b32_e32 v116, v122
	s_waitcnt vmcnt(0)
	v_mov_b32_e32 v117, v126
	v_mov_b32_e32 v126, v123
	v_mov_b32_e32 v122, v124
	v_mov_b32_e32 v123, v128
	v_mov_b32_e32 v128, v125
	v_pk_add_f32 v[118:119], v[136:137], v[118:119]
	v_pk_add_f32 v[114:115], v[114:115], v[120:121]
	v_pk_add_f32 v[116:117], v[116:117], v[126:127]
	v_pk_add_f32 v[120:121], v[122:123], v[128:129]
	v_pk_add_f32 v[114:115], v[118:119], v[114:115]
	v_pk_add_f32 v[116:117], v[116:117], v[120:121]
	s_nop 0
	v_pk_add_f32 v[114:115], v[114:115], v[116:117]
	v_mad_i64_i32 v[116:117], s[2:3], v134, s4, 0
	v_add_f32_e32 v114, v114, v115
	v_fma_f32 v114, s6, v114, v132
	v_rsq_f32_e32 v114, v114
	v_lshl_add_u64 v[116:117], v[116:117], 1, s[8:9]
	v_lshl_add_u64 v[116:117], v[116:117], 0, v[130:131]
	v_pk_mul_f32 v[110:111], v[110:111], v[114:115] op_sel_hi:[1,0]
	v_pk_mul_f32 v[112:113], v[112:113], v[114:115] op_sel_hi:[1,0]
	v_pk_mul_f32 v[106:107], v[106:107], v[114:115] op_sel_hi:[1,0]
	v_pk_mul_f32 v[108:109], v[108:109], v[114:115] op_sel_hi:[1,0]
	v_pk_mul_f32 v[102:103], v[102:103], v[114:115] op_sel_hi:[1,0]
	v_pk_mul_f32 v[104:105], v[104:105], v[114:115] op_sel_hi:[1,0]
	v_pk_mul_f32 v[98:99], v[98:99], v[114:115] op_sel_hi:[1,0]
	v_pk_mul_f32 v[100:101], v[100:101], v[114:115] op_sel_hi:[1,0]
	v_pk_mul_f32 v[118:119], v[110:111], s[44:45]
	v_pk_mul_f32 v[120:121], v[112:113], s[44:45]
	v_pk_mul_f32 v[122:123], v[106:107], s[44:45]
	v_pk_mul_f32 v[124:125], v[108:109], s[44:45]
	v_pk_fma_f32 v[118:119], v[110:111], v[118:119], s[46:47] neg_lo:[1,0,0] neg_hi:[1,0,0]
	v_pk_fma_f32 v[120:121], v[112:113], v[120:121], s[46:47] neg_lo:[1,0,0] neg_hi:[1,0,0]
	v_pk_fma_f32 v[122:123], v[106:107], v[122:123], s[46:47] neg_lo:[1,0,0] neg_hi:[1,0,0]
	v_pk_fma_f32 v[124:125], v[108:109], v[124:125], s[46:47] neg_lo:[1,0,0] neg_hi:[1,0,0]
	v_pk_mul_f32 v[118:119], v[110:111], v[118:119]
	v_pk_mul_f32 v[120:121], v[112:113], v[120:121]
	v_pk_mul_f32 v[122:123], v[106:107], v[122:123]
	v_pk_mul_f32 v[124:125], v[108:109], v[124:125]
	v_exp_f32_e32 v118, v118
	v_exp_f32_e32 v119, v119
	v_exp_f32_e32 v120, v120
	v_exp_f32_e32 v121, v121
	v_exp_f32_e32 v122, v122
	v_exp_f32_e32 v123, v123
	v_exp_f32_e32 v124, v124
	v_exp_f32_e32 v125, v125
	v_pk_add_f32 v[118:119], v[118:119], s[48:49]
	v_pk_add_f32 v[120:121], v[120:121], s[48:49]
	v_pk_add_f32 v[122:123], v[122:123], s[48:49]
	v_pk_add_f32 v[124:125], v[124:125], s[48:49]
	v_rcp_f32_e32 v118, v118
	v_rcp_f32_e32 v119, v119
	v_rcp_f32_e32 v120, v120
	v_rcp_f32_e32 v121, v121
	v_rcp_f32_e32 v122, v122
	v_rcp_f32_e32 v123, v123
	v_rcp_f32_e32 v124, v124
	v_rcp_f32_e32 v125, v125
	s_nop 0
	v_pk_mul_f32 v[110:111], v[110:111], v[118:119]
	v_pk_mul_f32 v[112:113], v[112:113], v[120:121]
	v_pk_mul_f32 v[106:107], v[106:107], v[122:123]
	v_pk_mul_f32 v[108:109], v[108:109], v[124:125]
	v_cvt_pk_bf16_f32 v118, v110, v111
	v_cvt_pk_bf16_f32 v119, v112, v113
	v_cvt_pk_bf16_f32 v120, v106, v107
	v_cvt_pk_bf16_f32 v121, v108, v109
	global_store_dwordx4 v[116:117], v[118:121], off
	v_pk_mul_f32 v[110:111], v[102:103], s[44:45]
	v_pk_mul_f32 v[112:113], v[104:105], s[44:45]
	v_pk_mul_f32 v[106:107], v[98:99], s[44:45]
	v_pk_mul_f32 v[108:109], v[100:101], s[44:45]
	v_pk_fma_f32 v[110:111], v[102:103], v[110:111], s[46:47] neg_lo:[1,0,0] neg_hi:[1,0,0]
	v_pk_fma_f32 v[112:113], v[104:105], v[112:113], s[46:47] neg_lo:[1,0,0] neg_hi:[1,0,0]
	v_pk_fma_f32 v[106:107], v[98:99], v[106:107], s[46:47] neg_lo:[1,0,0] neg_hi:[1,0,0]
	v_pk_fma_f32 v[108:109], v[100:101], v[108:109], s[46:47] neg_lo:[1,0,0] neg_hi:[1,0,0]
	v_pk_mul_f32 v[110:111], v[102:103], v[110:111]
	v_pk_mul_f32 v[112:113], v[104:105], v[112:113]
	v_pk_mul_f32 v[106:107], v[98:99], v[106:107]
	v_pk_mul_f32 v[108:109], v[100:101], v[108:109]
	v_exp_f32_e32 v110, v110
	v_exp_f32_e32 v111, v111
	v_exp_f32_e32 v112, v112
	v_exp_f32_e32 v113, v113
	v_exp_f32_e32 v106, v106
	v_exp_f32_e32 v107, v107
	v_exp_f32_e32 v108, v108
	v_exp_f32_e32 v109, v109
	v_pk_add_f32 v[110:111], v[110:111], s[48:49]
	v_pk_add_f32 v[112:113], v[112:113], s[48:49]
	v_pk_add_f32 v[106:107], v[106:107], s[48:49]
	v_pk_add_f32 v[108:109], v[108:109], s[48:49]
	v_rcp_f32_e32 v110, v110
	v_rcp_f32_e32 v111, v111
	v_rcp_f32_e32 v112, v112
	v_rcp_f32_e32 v113, v113
	v_rcp_f32_e32 v106, v106
	v_rcp_f32_e32 v107, v107
	v_rcp_f32_e32 v108, v108
	v_rcp_f32_e32 v109, v109
	s_nop 0
	v_pk_mul_f32 v[102:103], v[102:103], v[110:111]
	v_pk_mul_f32 v[104:105], v[104:105], v[112:113]
	v_pk_mul_f32 v[98:99], v[98:99], v[106:107]
	v_pk_mul_f32 v[100:101], v[100:101], v[108:109]
	v_cvt_pk_bf16_f32 v122, v102, v103
	v_cvt_pk_bf16_f32 v123, v104, v105
	v_cvt_pk_bf16_f32 v124, v98, v99
	v_cvt_pk_bf16_f32 v125, v100, v101
	v_or_b32_e32 v114, 32, v0
	v_mov_b32_e32 v115, v1
	global_store_dwordx4 v[116:117], v[122:125], off offset:256
	s_nop 1
	v_lshlrev_b64 v[98:99], 6, v[114:115]
	v_lshl_add_u64 v[116:117], s[10:11], 0, v[98:99]
	global_load_dwordx4 v[98:101], v[116:117], off
	global_load_dwordx4 v[102:105], v[116:117], off offset:32
	global_load_dwordx4 v[106:109], v[116:117], off offset:16
	global_load_dwordx4 v[110:113], v[116:117], off offset:48
	s_waitcnt vmcnt(3)
	v_mov_b32_e32 v116, v98
	s_waitcnt vmcnt(2)
	v_mov_b32_e32 v117, v102
	v_mov_b32_e32 v102, v99
	v_pk_add_f32 v[98:99], v[116:117], v[102:103]
	v_mov_b32_e32 v102, v100
	v_mov_b32_e32 v103, v104
	v_mov_b32_e32 v104, v101
	v_pk_add_f32 v[100:101], v[102:103], v[104:105]
	s_waitcnt vmcnt(1)
	v_mov_b32_e32 v102, v108
	v_pk_add_f32 v[98:99], v[98:99], v[100:101]
	v_mov_b32_e32 v100, v106
	s_waitcnt vmcnt(0)
	v_mov_b32_e32 v101, v110
	v_mov_b32_e32 v110, v107
	v_mov_b32_e32 v103, v112
	v_mov_b32_e32 v112, v109
	v_pk_add_f32 v[100:101], v[100:101], v[110:111]
	v_pk_add_f32 v[102:103], v[102:103], v[112:113]
	s_nop 0
	v_pk_add_f32 v[100:101], v[100:101], v[102:103]
	s_nop 0
	v_pk_add_f32 v[98:99], v[98:99], v[100:101]
	v_mad_i64_i32 v[100:101], s[2:3], v114, s4, 0
	v_add_f32_e32 v98, v98, v99
	v_fma_f32 v98, s6, v98, v132
	v_rsq_f32_e32 v98, v98
	v_lshl_add_u64 v[100:101], v[100:101], 1, s[8:9]
	v_lshl_add_u64 v[100:101], v[100:101], 0, v[130:131]
	v_pk_mul_f32 v[94:95], v[94:95], v[98:99] op_sel_hi:[1,0]
	v_pk_mul_f32 v[96:97], v[96:97], v[98:99] op_sel_hi:[1,0]
	v_pk_mul_f32 v[90:91], v[90:91], v[98:99] op_sel_hi:[1,0]
	v_pk_mul_f32 v[92:93], v[92:93], v[98:99] op_sel_hi:[1,0]
	v_pk_mul_f32 v[86:87], v[86:87], v[98:99] op_sel_hi:[1,0]
	v_pk_mul_f32 v[88:89], v[88:89], v[98:99] op_sel_hi:[1,0]
	v_pk_mul_f32 v[82:83], v[82:83], v[98:99] op_sel_hi:[1,0]
	v_pk_mul_f32 v[84:85], v[84:85], v[98:99] op_sel_hi:[1,0]
	v_pk_mul_f32 v[102:103], v[94:95], s[44:45]
	v_pk_mul_f32 v[104:105], v[96:97], s[44:45]
	v_pk_mul_f32 v[106:107], v[90:91], s[44:45]
	v_pk_mul_f32 v[108:109], v[92:93], s[44:45]
	v_pk_fma_f32 v[102:103], v[94:95], v[102:103], s[46:47] neg_lo:[1,0,0] neg_hi:[1,0,0]
	v_pk_fma_f32 v[104:105], v[96:97], v[104:105], s[46:47] neg_lo:[1,0,0] neg_hi:[1,0,0]
	v_pk_fma_f32 v[106:107], v[90:91], v[106:107], s[46:47] neg_lo:[1,0,0] neg_hi:[1,0,0]
	v_pk_fma_f32 v[108:109], v[92:93], v[108:109], s[46:47] neg_lo:[1,0,0] neg_hi:[1,0,0]
	v_pk_mul_f32 v[102:103], v[94:95], v[102:103]
	v_pk_mul_f32 v[104:105], v[96:97], v[104:105]
	v_pk_mul_f32 v[106:107], v[90:91], v[106:107]
	v_pk_mul_f32 v[108:109], v[92:93], v[108:109]
	v_exp_f32_e32 v102, v102
	v_exp_f32_e32 v103, v103
	v_exp_f32_e32 v104, v104
	v_exp_f32_e32 v105, v105
	v_exp_f32_e32 v106, v106
	v_exp_f32_e32 v107, v107
	v_exp_f32_e32 v108, v108
	v_exp_f32_e32 v109, v109
	v_pk_add_f32 v[102:103], v[102:103], s[48:49]
	v_pk_add_f32 v[104:105], v[104:105], s[48:49]
	v_pk_add_f32 v[106:107], v[106:107], s[48:49]
	v_pk_add_f32 v[108:109], v[108:109], s[48:49]
	v_rcp_f32_e32 v102, v102
	v_rcp_f32_e32 v103, v103
	v_rcp_f32_e32 v104, v104
	v_rcp_f32_e32 v105, v105
	v_rcp_f32_e32 v106, v106
	v_rcp_f32_e32 v107, v107
	v_rcp_f32_e32 v108, v108
	v_rcp_f32_e32 v109, v109
	s_nop 0
	v_pk_mul_f32 v[94:95], v[94:95], v[102:103]
	v_pk_mul_f32 v[96:97], v[96:97], v[104:105]
	v_pk_mul_f32 v[90:91], v[90:91], v[106:107]
	v_pk_mul_f32 v[92:93], v[92:93], v[108:109]
	v_cvt_pk_bf16_f32 v102, v94, v95
	v_cvt_pk_bf16_f32 v103, v96, v97
	v_cvt_pk_bf16_f32 v104, v90, v91
	v_cvt_pk_bf16_f32 v105, v92, v93
	global_store_dwordx4 v[100:101], v[102:105], off
	v_pk_mul_f32 v[94:95], v[86:87], s[44:45]
	v_pk_mul_f32 v[96:97], v[88:89], s[44:45]
	v_pk_mul_f32 v[90:91], v[82:83], s[44:45]
	v_pk_mul_f32 v[92:93], v[84:85], s[44:45]
	v_pk_fma_f32 v[94:95], v[86:87], v[94:95], s[46:47] neg_lo:[1,0,0] neg_hi:[1,0,0]
	v_pk_fma_f32 v[96:97], v[88:89], v[96:97], s[46:47] neg_lo:[1,0,0] neg_hi:[1,0,0]
	v_pk_fma_f32 v[90:91], v[82:83], v[90:91], s[46:47] neg_lo:[1,0,0] neg_hi:[1,0,0]
	v_pk_fma_f32 v[92:93], v[84:85], v[92:93], s[46:47] neg_lo:[1,0,0] neg_hi:[1,0,0]
	v_pk_mul_f32 v[94:95], v[86:87], v[94:95]
	v_pk_mul_f32 v[96:97], v[88:89], v[96:97]
	v_pk_mul_f32 v[90:91], v[82:83], v[90:91]
	v_pk_mul_f32 v[92:93], v[84:85], v[92:93]
	v_exp_f32_e32 v94, v94
	v_exp_f32_e32 v95, v95
	v_exp_f32_e32 v96, v96
	v_exp_f32_e32 v97, v97
	v_exp_f32_e32 v90, v90
	v_exp_f32_e32 v91, v91
	v_exp_f32_e32 v92, v92
	v_exp_f32_e32 v93, v93
	v_pk_add_f32 v[94:95], v[94:95], s[48:49]
	v_pk_add_f32 v[96:97], v[96:97], s[48:49]
	v_pk_add_f32 v[90:91], v[90:91], s[48:49]
	v_pk_add_f32 v[92:93], v[92:93], s[48:49]
	v_rcp_f32_e32 v94, v94
	v_rcp_f32_e32 v95, v95
	v_rcp_f32_e32 v96, v96
	v_rcp_f32_e32 v97, v97
	v_rcp_f32_e32 v90, v90
	v_rcp_f32_e32 v91, v91
	v_rcp_f32_e32 v92, v92
	v_rcp_f32_e32 v93, v93
	s_nop 0
	v_pk_mul_f32 v[86:87], v[86:87], v[94:95]
	v_pk_mul_f32 v[88:89], v[88:89], v[96:97]
	v_pk_mul_f32 v[82:83], v[82:83], v[90:91]
	v_pk_mul_f32 v[84:85], v[84:85], v[92:93]
	v_cvt_pk_bf16_f32 v106, v86, v87
	v_cvt_pk_bf16_f32 v107, v88, v89
	v_cvt_pk_bf16_f32 v108, v82, v83
	v_cvt_pk_bf16_f32 v109, v84, v85
	v_or_b32_e32 v98, 48, v0
	v_mov_b32_e32 v99, v1
	global_store_dwordx4 v[100:101], v[106:109], off offset:256
	s_nop 1
	v_lshlrev_b64 v[82:83], 6, v[98:99]
	v_lshl_add_u64 v[100:101], s[10:11], 0, v[82:83]
	global_load_dwordx4 v[82:85], v[100:101], off
	global_load_dwordx4 v[86:89], v[100:101], off offset:32
	global_load_dwordx4 v[90:93], v[100:101], off offset:16
	global_load_dwordx4 v[94:97], v[100:101], off offset:48
	s_waitcnt vmcnt(3)
	v_mov_b32_e32 v100, v82
	s_waitcnt vmcnt(2)
	v_mov_b32_e32 v101, v86
	v_mov_b32_e32 v86, v83
	v_pk_add_f32 v[82:83], v[100:101], v[86:87]
	v_mov_b32_e32 v86, v84
	v_mov_b32_e32 v87, v88
	v_mov_b32_e32 v88, v85
	v_pk_add_f32 v[84:85], v[86:87], v[88:89]
	s_waitcnt vmcnt(1)
	v_mov_b32_e32 v86, v92
	v_pk_add_f32 v[82:83], v[82:83], v[84:85]
	v_mov_b32_e32 v84, v90
	s_waitcnt vmcnt(0)
	v_mov_b32_e32 v85, v94
	v_mov_b32_e32 v94, v91
	v_mov_b32_e32 v87, v96
	v_mov_b32_e32 v96, v93
	v_pk_add_f32 v[84:85], v[84:85], v[94:95]
	v_pk_add_f32 v[86:87], v[86:87], v[96:97]
	s_nop 0
	v_pk_add_f32 v[84:85], v[84:85], v[86:87]
	s_nop 0
	v_pk_add_f32 v[82:83], v[82:83], v[84:85]
	v_mad_i64_i32 v[84:85], s[2:3], v98, s4, 0
	v_add_f32_e32 v82, v82, v83
	v_fma_f32 v82, s6, v82, v132
	v_rsq_f32_e32 v82, v82
	v_lshl_add_u64 v[84:85], v[84:85], 1, s[8:9]
	v_lshl_add_u64 v[84:85], v[84:85], 0, v[130:131]
	v_pk_mul_f32 v[78:79], v[78:79], v[82:83] op_sel_hi:[1,0]
	v_pk_mul_f32 v[80:81], v[80:81], v[82:83] op_sel_hi:[1,0]
	v_pk_mul_f32 v[74:75], v[74:75], v[82:83] op_sel_hi:[1,0]
	v_pk_mul_f32 v[76:77], v[76:77], v[82:83] op_sel_hi:[1,0]
	v_pk_mul_f32 v[70:71], v[70:71], v[82:83] op_sel_hi:[1,0]
	v_pk_mul_f32 v[72:73], v[72:73], v[82:83] op_sel_hi:[1,0]
	v_pk_mul_f32 v[66:67], v[66:67], v[82:83] op_sel_hi:[1,0]
	v_pk_mul_f32 v[68:69], v[68:69], v[82:83] op_sel_hi:[1,0]
	v_pk_mul_f32 v[86:87], v[78:79], s[44:45]
	v_pk_mul_f32 v[88:89], v[80:81], s[44:45]
	v_pk_mul_f32 v[90:91], v[74:75], s[44:45]
	v_pk_mul_f32 v[92:93], v[76:77], s[44:45]
	v_pk_fma_f32 v[86:87], v[78:79], v[86:87], s[46:47] neg_lo:[1,0,0] neg_hi:[1,0,0]
	v_pk_fma_f32 v[88:89], v[80:81], v[88:89], s[46:47] neg_lo:[1,0,0] neg_hi:[1,0,0]
	v_pk_fma_f32 v[90:91], v[74:75], v[90:91], s[46:47] neg_lo:[1,0,0] neg_hi:[1,0,0]
	v_pk_fma_f32 v[92:93], v[76:77], v[92:93], s[46:47] neg_lo:[1,0,0] neg_hi:[1,0,0]
	v_pk_mul_f32 v[86:87], v[78:79], v[86:87]
	v_pk_mul_f32 v[88:89], v[80:81], v[88:89]
	v_pk_mul_f32 v[90:91], v[74:75], v[90:91]
	v_pk_mul_f32 v[92:93], v[76:77], v[92:93]
	v_exp_f32_e32 v86, v86
	v_exp_f32_e32 v87, v87
	v_exp_f32_e32 v88, v88
	v_exp_f32_e32 v89, v89
	v_exp_f32_e32 v90, v90
	v_exp_f32_e32 v91, v91
	v_exp_f32_e32 v92, v92
	v_exp_f32_e32 v93, v93
	v_pk_add_f32 v[86:87], v[86:87], s[48:49]
	v_pk_add_f32 v[88:89], v[88:89], s[48:49]
	v_pk_add_f32 v[90:91], v[90:91], s[48:49]
	v_pk_add_f32 v[92:93], v[92:93], s[48:49]
	v_rcp_f32_e32 v86, v86
	v_rcp_f32_e32 v87, v87
	v_rcp_f32_e32 v88, v88
	v_rcp_f32_e32 v89, v89
	v_rcp_f32_e32 v90, v90
	v_rcp_f32_e32 v91, v91
	v_rcp_f32_e32 v92, v92
	v_rcp_f32_e32 v93, v93
	s_nop 0
	v_pk_mul_f32 v[78:79], v[78:79], v[86:87]
	v_pk_mul_f32 v[80:81], v[80:81], v[88:89]
	v_pk_mul_f32 v[74:75], v[74:75], v[90:91]
	v_pk_mul_f32 v[76:77], v[76:77], v[92:93]
	v_cvt_pk_bf16_f32 v86, v78, v79
	v_cvt_pk_bf16_f32 v87, v80, v81
	v_cvt_pk_bf16_f32 v88, v74, v75
	v_cvt_pk_bf16_f32 v89, v76, v77
	global_store_dwordx4 v[84:85], v[86:89], off
	v_pk_mul_f32 v[78:79], v[70:71], s[44:45]
	v_pk_mul_f32 v[80:81], v[72:73], s[44:45]
	v_pk_mul_f32 v[74:75], v[66:67], s[44:45]
	v_pk_mul_f32 v[76:77], v[68:69], s[44:45]
	v_pk_fma_f32 v[78:79], v[70:71], v[78:79], s[46:47] neg_lo:[1,0,0] neg_hi:[1,0,0]
	v_pk_fma_f32 v[80:81], v[72:73], v[80:81], s[46:47] neg_lo:[1,0,0] neg_hi:[1,0,0]
	v_pk_fma_f32 v[74:75], v[66:67], v[74:75], s[46:47] neg_lo:[1,0,0] neg_hi:[1,0,0]
	v_pk_fma_f32 v[76:77], v[68:69], v[76:77], s[46:47] neg_lo:[1,0,0] neg_hi:[1,0,0]
	v_pk_mul_f32 v[78:79], v[70:71], v[78:79]
	v_pk_mul_f32 v[80:81], v[72:73], v[80:81]
	v_pk_mul_f32 v[74:75], v[66:67], v[74:75]
	v_pk_mul_f32 v[76:77], v[68:69], v[76:77]
	v_exp_f32_e32 v78, v78
	v_exp_f32_e32 v79, v79
	v_exp_f32_e32 v80, v80
	v_exp_f32_e32 v81, v81
	v_exp_f32_e32 v74, v74
	v_exp_f32_e32 v75, v75
	v_exp_f32_e32 v76, v76
	v_exp_f32_e32 v77, v77
	v_pk_add_f32 v[78:79], v[78:79], s[48:49]
	v_pk_add_f32 v[80:81], v[80:81], s[48:49]
	v_pk_add_f32 v[74:75], v[74:75], s[48:49]
	v_pk_add_f32 v[76:77], v[76:77], s[48:49]
	v_rcp_f32_e32 v78, v78
	v_rcp_f32_e32 v79, v79
	v_rcp_f32_e32 v80, v80
	v_rcp_f32_e32 v81, v81
	v_rcp_f32_e32 v74, v74
	v_rcp_f32_e32 v75, v75
	v_rcp_f32_e32 v76, v76
	v_rcp_f32_e32 v77, v77
	s_nop 0
	v_pk_mul_f32 v[70:71], v[70:71], v[78:79]
	v_pk_mul_f32 v[72:73], v[72:73], v[80:81]
	v_pk_mul_f32 v[66:67], v[66:67], v[74:75]
	v_pk_mul_f32 v[68:69], v[68:69], v[76:77]
	v_cvt_pk_bf16_f32 v90, v70, v71
	v_cvt_pk_bf16_f32 v91, v72, v73
	v_cvt_pk_bf16_f32 v92, v66, v67
	v_cvt_pk_bf16_f32 v93, v68, v69
	v_add_u32_e32 v82, 0x80, v0
	v_mov_b32_e32 v83, v1
	global_store_dwordx4 v[84:85], v[90:93], off offset:256
	s_nop 1
	v_lshlrev_b64 v[66:67], 6, v[82:83]
	v_lshl_add_u64 v[84:85], s[10:11], 0, v[66:67]
	global_load_dwordx4 v[66:69], v[84:85], off
	global_load_dwordx4 v[70:73], v[84:85], off offset:32
	global_load_dwordx4 v[74:77], v[84:85], off offset:16
	global_load_dwordx4 v[78:81], v[84:85], off offset:48
	s_waitcnt vmcnt(3)
	v_mov_b32_e32 v84, v66
	s_waitcnt vmcnt(2)
	v_mov_b32_e32 v85, v70
	v_mov_b32_e32 v70, v67
	v_pk_add_f32 v[66:67], v[84:85], v[70:71]
	v_mov_b32_e32 v70, v68
	v_mov_b32_e32 v71, v72
	v_mov_b32_e32 v72, v69
	v_pk_add_f32 v[68:69], v[70:71], v[72:73]
	s_waitcnt vmcnt(1)
	v_mov_b32_e32 v70, v76
	v_pk_add_f32 v[66:67], v[66:67], v[68:69]
	v_mov_b32_e32 v68, v74
	s_waitcnt vmcnt(0)
	v_mov_b32_e32 v69, v78
	v_mov_b32_e32 v78, v75
	v_mov_b32_e32 v71, v80
	v_mov_b32_e32 v80, v77
	v_pk_add_f32 v[68:69], v[68:69], v[78:79]
	v_pk_add_f32 v[70:71], v[70:71], v[80:81]
	s_nop 0
	v_pk_add_f32 v[68:69], v[68:69], v[70:71]
	s_nop 0
	v_pk_add_f32 v[66:67], v[66:67], v[68:69]
	v_mad_i64_i32 v[68:69], s[2:3], v82, s4, 0
	v_add_f32_e32 v66, v66, v67
	v_fma_f32 v66, s6, v66, v132
	v_rsq_f32_e32 v66, v66
	v_lshl_add_u64 v[68:69], v[68:69], 1, s[8:9]
	v_lshl_add_u64 v[68:69], v[68:69], 0, v[130:131]
	v_pk_mul_f32 v[62:63], v[62:63], v[66:67] op_sel_hi:[1,0]
	v_pk_mul_f32 v[64:65], v[64:65], v[66:67] op_sel_hi:[1,0]
	v_pk_mul_f32 v[58:59], v[58:59], v[66:67] op_sel_hi:[1,0]
	v_pk_mul_f32 v[60:61], v[60:61], v[66:67] op_sel_hi:[1,0]
	v_pk_mul_f32 v[54:55], v[54:55], v[66:67] op_sel_hi:[1,0]
	v_pk_mul_f32 v[56:57], v[56:57], v[66:67] op_sel_hi:[1,0]
	v_pk_mul_f32 v[50:51], v[50:51], v[66:67] op_sel_hi:[1,0]
	v_pk_mul_f32 v[52:53], v[52:53], v[66:67] op_sel_hi:[1,0]
	v_pk_mul_f32 v[70:71], v[62:63], s[44:45]
	v_pk_mul_f32 v[72:73], v[64:65], s[44:45]
	v_pk_mul_f32 v[74:75], v[58:59], s[44:45]
	v_pk_mul_f32 v[76:77], v[60:61], s[44:45]
	v_pk_fma_f32 v[70:71], v[62:63], v[70:71], s[46:47] neg_lo:[1,0,0] neg_hi:[1,0,0]
	v_pk_fma_f32 v[72:73], v[64:65], v[72:73], s[46:47] neg_lo:[1,0,0] neg_hi:[1,0,0]
	v_pk_fma_f32 v[74:75], v[58:59], v[74:75], s[46:47] neg_lo:[1,0,0] neg_hi:[1,0,0]
	v_pk_fma_f32 v[76:77], v[60:61], v[76:77], s[46:47] neg_lo:[1,0,0] neg_hi:[1,0,0]
	v_pk_mul_f32 v[70:71], v[62:63], v[70:71]
	v_pk_mul_f32 v[72:73], v[64:65], v[72:73]
	v_pk_mul_f32 v[74:75], v[58:59], v[74:75]
	v_pk_mul_f32 v[76:77], v[60:61], v[76:77]
	v_exp_f32_e32 v70, v70
	v_exp_f32_e32 v71, v71
	v_exp_f32_e32 v72, v72
	v_exp_f32_e32 v73, v73
	v_exp_f32_e32 v74, v74
	v_exp_f32_e32 v75, v75
	v_exp_f32_e32 v76, v76
	v_exp_f32_e32 v77, v77
	v_pk_add_f32 v[70:71], v[70:71], s[48:49]
	v_pk_add_f32 v[72:73], v[72:73], s[48:49]
	v_pk_add_f32 v[74:75], v[74:75], s[48:49]
	v_pk_add_f32 v[76:77], v[76:77], s[48:49]
	v_rcp_f32_e32 v70, v70
	v_rcp_f32_e32 v71, v71
	v_rcp_f32_e32 v72, v72
	v_rcp_f32_e32 v73, v73
	v_rcp_f32_e32 v74, v74
	v_rcp_f32_e32 v75, v75
	v_rcp_f32_e32 v76, v76
	v_rcp_f32_e32 v77, v77
	s_nop 0
	v_pk_mul_f32 v[62:63], v[62:63], v[70:71]
	v_pk_mul_f32 v[64:65], v[64:65], v[72:73]
	v_pk_mul_f32 v[58:59], v[58:59], v[74:75]
	v_pk_mul_f32 v[60:61], v[60:61], v[76:77]
	v_cvt_pk_bf16_f32 v70, v62, v63
	v_cvt_pk_bf16_f32 v71, v64, v65
	v_cvt_pk_bf16_f32 v72, v58, v59
	v_cvt_pk_bf16_f32 v73, v60, v61
	global_store_dwordx4 v[68:69], v[70:73], off
	v_pk_mul_f32 v[62:63], v[54:55], s[44:45]
	v_pk_mul_f32 v[64:65], v[56:57], s[44:45]
	v_pk_mul_f32 v[58:59], v[50:51], s[44:45]
	v_pk_mul_f32 v[60:61], v[52:53], s[44:45]
	v_pk_fma_f32 v[62:63], v[54:55], v[62:63], s[46:47] neg_lo:[1,0,0] neg_hi:[1,0,0]
	v_pk_fma_f32 v[64:65], v[56:57], v[64:65], s[46:47] neg_lo:[1,0,0] neg_hi:[1,0,0]
	v_pk_fma_f32 v[58:59], v[50:51], v[58:59], s[46:47] neg_lo:[1,0,0] neg_hi:[1,0,0]
	v_pk_fma_f32 v[60:61], v[52:53], v[60:61], s[46:47] neg_lo:[1,0,0] neg_hi:[1,0,0]
	v_pk_mul_f32 v[62:63], v[54:55], v[62:63]
	v_pk_mul_f32 v[64:65], v[56:57], v[64:65]
	v_pk_mul_f32 v[58:59], v[50:51], v[58:59]
	v_pk_mul_f32 v[60:61], v[52:53], v[60:61]
	v_exp_f32_e32 v62, v62
	v_exp_f32_e32 v63, v63
	v_exp_f32_e32 v64, v64
	v_exp_f32_e32 v65, v65
	v_exp_f32_e32 v58, v58
	v_exp_f32_e32 v59, v59
	v_exp_f32_e32 v60, v60
	v_exp_f32_e32 v61, v61
	v_pk_add_f32 v[62:63], v[62:63], s[48:49]
	v_pk_add_f32 v[64:65], v[64:65], s[48:49]
	v_pk_add_f32 v[58:59], v[58:59], s[48:49]
	v_pk_add_f32 v[60:61], v[60:61], s[48:49]
	v_rcp_f32_e32 v62, v62
	v_rcp_f32_e32 v63, v63
	v_rcp_f32_e32 v64, v64
	v_rcp_f32_e32 v65, v65
	v_rcp_f32_e32 v58, v58
	v_rcp_f32_e32 v59, v59
	v_rcp_f32_e32 v60, v60
	v_rcp_f32_e32 v61, v61
	s_nop 0
	v_pk_mul_f32 v[54:55], v[54:55], v[62:63]
	v_pk_mul_f32 v[56:57], v[56:57], v[64:65]
	v_pk_mul_f32 v[50:51], v[50:51], v[58:59]
	v_pk_mul_f32 v[52:53], v[52:53], v[60:61]
	v_cvt_pk_bf16_f32 v74, v54, v55
	v_cvt_pk_bf16_f32 v75, v56, v57
	v_cvt_pk_bf16_f32 v76, v50, v51
	v_cvt_pk_bf16_f32 v77, v52, v53
	v_add_u32_e32 v66, 0x90, v0
	v_mov_b32_e32 v67, v1
	global_store_dwordx4 v[68:69], v[74:77], off offset:256
	s_nop 1
	v_lshlrev_b64 v[50:51], 6, v[66:67]
	v_lshl_add_u64 v[68:69], s[10:11], 0, v[50:51]
	global_load_dwordx4 v[50:53], v[68:69], off
	global_load_dwordx4 v[54:57], v[68:69], off offset:32
	global_load_dwordx4 v[58:61], v[68:69], off offset:16
	global_load_dwordx4 v[62:65], v[68:69], off offset:48
	s_waitcnt vmcnt(3)
	v_mov_b32_e32 v68, v50
	s_waitcnt vmcnt(2)
	v_mov_b32_e32 v69, v54
	v_mov_b32_e32 v54, v51
	v_pk_add_f32 v[50:51], v[68:69], v[54:55]
	v_mov_b32_e32 v54, v52
	v_mov_b32_e32 v55, v56
	v_mov_b32_e32 v56, v53
	v_pk_add_f32 v[52:53], v[54:55], v[56:57]
	s_waitcnt vmcnt(1)
	v_mov_b32_e32 v54, v60
	v_pk_add_f32 v[50:51], v[50:51], v[52:53]
	v_mov_b32_e32 v52, v58
	s_waitcnt vmcnt(0)
	v_mov_b32_e32 v53, v62
	v_mov_b32_e32 v62, v59
	v_mov_b32_e32 v55, v64
	v_mov_b32_e32 v64, v61
	v_pk_add_f32 v[52:53], v[52:53], v[62:63]
	v_pk_add_f32 v[54:55], v[54:55], v[64:65]
	s_nop 0
	v_pk_add_f32 v[52:53], v[52:53], v[54:55]
	s_nop 0
	v_pk_add_f32 v[50:51], v[50:51], v[52:53]
	v_mad_i64_i32 v[52:53], s[2:3], v66, s4, 0
	v_add_f32_e32 v50, v50, v51
	v_fma_f32 v50, s6, v50, v132
	v_rsq_f32_e32 v50, v50
	v_lshl_add_u64 v[52:53], v[52:53], 1, s[8:9]
	v_lshl_add_u64 v[52:53], v[52:53], 0, v[130:131]
	v_pk_mul_f32 v[46:47], v[46:47], v[50:51] op_sel_hi:[1,0]
	v_pk_mul_f32 v[48:49], v[48:49], v[50:51] op_sel_hi:[1,0]
	v_pk_mul_f32 v[42:43], v[42:43], v[50:51] op_sel_hi:[1,0]
	v_pk_mul_f32 v[44:45], v[44:45], v[50:51] op_sel_hi:[1,0]
	v_pk_mul_f32 v[38:39], v[38:39], v[50:51] op_sel_hi:[1,0]
	v_pk_mul_f32 v[40:41], v[40:41], v[50:51] op_sel_hi:[1,0]
	v_pk_mul_f32 v[34:35], v[34:35], v[50:51] op_sel_hi:[1,0]
	v_pk_mul_f32 v[36:37], v[36:37], v[50:51] op_sel_hi:[1,0]
	v_pk_mul_f32 v[54:55], v[46:47], s[44:45]
	v_pk_mul_f32 v[56:57], v[48:49], s[44:45]
	v_pk_mul_f32 v[58:59], v[42:43], s[44:45]
	v_pk_mul_f32 v[60:61], v[44:45], s[44:45]
	v_pk_fma_f32 v[54:55], v[46:47], v[54:55], s[46:47] neg_lo:[1,0,0] neg_hi:[1,0,0]
	v_pk_fma_f32 v[56:57], v[48:49], v[56:57], s[46:47] neg_lo:[1,0,0] neg_hi:[1,0,0]
	v_pk_fma_f32 v[58:59], v[42:43], v[58:59], s[46:47] neg_lo:[1,0,0] neg_hi:[1,0,0]
	v_pk_fma_f32 v[60:61], v[44:45], v[60:61], s[46:47] neg_lo:[1,0,0] neg_hi:[1,0,0]
	v_pk_mul_f32 v[54:55], v[46:47], v[54:55]
	v_pk_mul_f32 v[56:57], v[48:49], v[56:57]
	v_pk_mul_f32 v[58:59], v[42:43], v[58:59]
	v_pk_mul_f32 v[60:61], v[44:45], v[60:61]
	v_exp_f32_e32 v54, v54
	v_exp_f32_e32 v55, v55
	v_exp_f32_e32 v56, v56
	v_exp_f32_e32 v57, v57
	v_exp_f32_e32 v58, v58
	v_exp_f32_e32 v59, v59
	v_exp_f32_e32 v60, v60
	v_exp_f32_e32 v61, v61
	v_pk_add_f32 v[54:55], v[54:55], s[48:49]
	v_pk_add_f32 v[56:57], v[56:57], s[48:49]
	v_pk_add_f32 v[58:59], v[58:59], s[48:49]
	v_pk_add_f32 v[60:61], v[60:61], s[48:49]
	v_rcp_f32_e32 v54, v54
	v_rcp_f32_e32 v55, v55
	v_rcp_f32_e32 v56, v56
	v_rcp_f32_e32 v57, v57
	v_rcp_f32_e32 v58, v58
	v_rcp_f32_e32 v59, v59
	v_rcp_f32_e32 v60, v60
	v_rcp_f32_e32 v61, v61
	s_nop 0
	v_pk_mul_f32 v[46:47], v[46:47], v[54:55]
	v_pk_mul_f32 v[48:49], v[48:49], v[56:57]
	v_pk_mul_f32 v[42:43], v[42:43], v[58:59]
	v_pk_mul_f32 v[44:45], v[44:45], v[60:61]
	v_cvt_pk_bf16_f32 v54, v46, v47
	v_cvt_pk_bf16_f32 v55, v48, v49
	v_cvt_pk_bf16_f32 v56, v42, v43
	v_cvt_pk_bf16_f32 v57, v44, v45
	global_store_dwordx4 v[52:53], v[54:57], off
	v_pk_mul_f32 v[46:47], v[38:39], s[44:45]
	v_pk_mul_f32 v[48:49], v[40:41], s[44:45]
	v_pk_mul_f32 v[42:43], v[34:35], s[44:45]
	v_pk_mul_f32 v[44:45], v[36:37], s[44:45]
	v_pk_fma_f32 v[46:47], v[38:39], v[46:47], s[46:47] neg_lo:[1,0,0] neg_hi:[1,0,0]
	v_pk_fma_f32 v[48:49], v[40:41], v[48:49], s[46:47] neg_lo:[1,0,0] neg_hi:[1,0,0]
	v_pk_fma_f32 v[42:43], v[34:35], v[42:43], s[46:47] neg_lo:[1,0,0] neg_hi:[1,0,0]
	v_pk_fma_f32 v[44:45], v[36:37], v[44:45], s[46:47] neg_lo:[1,0,0] neg_hi:[1,0,0]
	v_pk_mul_f32 v[46:47], v[38:39], v[46:47]
	v_pk_mul_f32 v[48:49], v[40:41], v[48:49]
	v_pk_mul_f32 v[42:43], v[34:35], v[42:43]
	v_pk_mul_f32 v[44:45], v[36:37], v[44:45]
	v_exp_f32_e32 v46, v46
	v_exp_f32_e32 v47, v47
	v_exp_f32_e32 v48, v48
	v_exp_f32_e32 v49, v49
	v_exp_f32_e32 v42, v42
	v_exp_f32_e32 v43, v43
	v_exp_f32_e32 v44, v44
	v_exp_f32_e32 v45, v45
	v_pk_add_f32 v[46:47], v[46:47], s[48:49]
	v_pk_add_f32 v[48:49], v[48:49], s[48:49]
	v_pk_add_f32 v[42:43], v[42:43], s[48:49]
	v_pk_add_f32 v[44:45], v[44:45], s[48:49]
	v_rcp_f32_e32 v46, v46
	v_rcp_f32_e32 v47, v47
	v_rcp_f32_e32 v48, v48
	v_rcp_f32_e32 v49, v49
	v_rcp_f32_e32 v42, v42
	v_rcp_f32_e32 v43, v43
	v_rcp_f32_e32 v44, v44
	v_rcp_f32_e32 v45, v45
	s_nop 0
	v_pk_mul_f32 v[38:39], v[38:39], v[46:47]
	v_pk_mul_f32 v[40:41], v[40:41], v[48:49]
	v_pk_mul_f32 v[34:35], v[34:35], v[42:43]
	v_pk_mul_f32 v[36:37], v[36:37], v[44:45]
	v_cvt_pk_bf16_f32 v58, v38, v39
	v_cvt_pk_bf16_f32 v59, v40, v41
	v_cvt_pk_bf16_f32 v60, v34, v35
	v_cvt_pk_bf16_f32 v61, v36, v37
	v_add_u32_e32 v50, 0xa0, v0
	v_mov_b32_e32 v51, v1
	global_store_dwordx4 v[52:53], v[58:61], off offset:256
	v_add_u32_e32 v0, 0xb0, v0
	s_nop 0
	v_lshlrev_b64 v[34:35], 6, v[50:51]
	v_lshl_add_u64 v[52:53], s[10:11], 0, v[34:35]
	global_load_dwordx4 v[34:37], v[52:53], off
	global_load_dwordx4 v[38:41], v[52:53], off offset:32
	global_load_dwordx4 v[42:45], v[52:53], off offset:16
	global_load_dwordx4 v[46:49], v[52:53], off offset:48
	s_waitcnt vmcnt(3)
	v_mov_b32_e32 v52, v34
	s_waitcnt vmcnt(2)
	v_mov_b32_e32 v53, v38
	v_mov_b32_e32 v38, v35
	v_pk_add_f32 v[34:35], v[52:53], v[38:39]
	v_mov_b32_e32 v38, v36
	v_mov_b32_e32 v39, v40
	v_mov_b32_e32 v40, v37
	v_pk_add_f32 v[36:37], v[38:39], v[40:41]
	s_waitcnt vmcnt(1)
	v_mov_b32_e32 v38, v44
	v_pk_add_f32 v[34:35], v[34:35], v[36:37]
	v_mov_b32_e32 v36, v42
	s_waitcnt vmcnt(0)
	v_mov_b32_e32 v37, v46
	v_mov_b32_e32 v46, v43
	v_mov_b32_e32 v39, v48
	v_mov_b32_e32 v48, v45
	v_pk_add_f32 v[36:37], v[36:37], v[46:47]
	v_pk_add_f32 v[38:39], v[38:39], v[48:49]
	s_nop 0
	v_pk_add_f32 v[36:37], v[36:37], v[38:39]
	s_nop 0
	v_pk_add_f32 v[34:35], v[34:35], v[36:37]
	v_mad_i64_i32 v[36:37], s[2:3], v50, s4, 0
	v_add_f32_e32 v34, v34, v35
	v_fma_f32 v34, s6, v34, v132
	v_rsq_f32_e32 v34, v34
	v_lshl_add_u64 v[36:37], v[36:37], 1, s[8:9]
	v_lshl_add_u64 v[36:37], v[36:37], 0, v[130:131]
	v_pk_mul_f32 v[30:31], v[30:31], v[34:35] op_sel_hi:[1,0]
	v_pk_mul_f32 v[32:33], v[32:33], v[34:35] op_sel_hi:[1,0]
	v_pk_mul_f32 v[26:27], v[26:27], v[34:35] op_sel_hi:[1,0]
	v_pk_mul_f32 v[28:29], v[28:29], v[34:35] op_sel_hi:[1,0]
	v_pk_mul_f32 v[22:23], v[22:23], v[34:35] op_sel_hi:[1,0]
	v_pk_mul_f32 v[24:25], v[24:25], v[34:35] op_sel_hi:[1,0]
	v_pk_mul_f32 v[18:19], v[18:19], v[34:35] op_sel_hi:[1,0]
	v_pk_mul_f32 v[20:21], v[20:21], v[34:35] op_sel_hi:[1,0]
	v_pk_mul_f32 v[38:39], v[30:31], s[44:45]
	v_pk_mul_f32 v[40:41], v[32:33], s[44:45]
	v_pk_mul_f32 v[42:43], v[26:27], s[44:45]
	v_pk_mul_f32 v[44:45], v[28:29], s[44:45]
	v_pk_fma_f32 v[38:39], v[30:31], v[38:39], s[46:47] neg_lo:[1,0,0] neg_hi:[1,0,0]
	v_pk_fma_f32 v[40:41], v[32:33], v[40:41], s[46:47] neg_lo:[1,0,0] neg_hi:[1,0,0]
	v_pk_fma_f32 v[42:43], v[26:27], v[42:43], s[46:47] neg_lo:[1,0,0] neg_hi:[1,0,0]
	v_pk_fma_f32 v[44:45], v[28:29], v[44:45], s[46:47] neg_lo:[1,0,0] neg_hi:[1,0,0]
	v_pk_mul_f32 v[38:39], v[30:31], v[38:39]
	v_pk_mul_f32 v[40:41], v[32:33], v[40:41]
	v_pk_mul_f32 v[42:43], v[26:27], v[42:43]
	v_pk_mul_f32 v[44:45], v[28:29], v[44:45]
	v_exp_f32_e32 v38, v38
	v_exp_f32_e32 v39, v39
	v_exp_f32_e32 v40, v40
	v_exp_f32_e32 v41, v41
	v_exp_f32_e32 v42, v42
	v_exp_f32_e32 v43, v43
	v_exp_f32_e32 v44, v44
	v_exp_f32_e32 v45, v45
	v_pk_add_f32 v[38:39], v[38:39], s[48:49]
	v_pk_add_f32 v[40:41], v[40:41], s[48:49]
	v_pk_add_f32 v[42:43], v[42:43], s[48:49]
	v_pk_add_f32 v[44:45], v[44:45], s[48:49]
	v_rcp_f32_e32 v38, v38
	v_rcp_f32_e32 v39, v39
	v_rcp_f32_e32 v40, v40
	v_rcp_f32_e32 v41, v41
	v_rcp_f32_e32 v42, v42
	v_rcp_f32_e32 v43, v43
	v_rcp_f32_e32 v44, v44
	v_rcp_f32_e32 v45, v45
	s_nop 0
	v_pk_mul_f32 v[30:31], v[30:31], v[38:39]
	v_pk_mul_f32 v[32:33], v[32:33], v[40:41]
	v_pk_mul_f32 v[26:27], v[26:27], v[42:43]
	v_pk_mul_f32 v[28:29], v[28:29], v[44:45]
	v_cvt_pk_bf16_f32 v38, v30, v31
	v_cvt_pk_bf16_f32 v39, v32, v33
	v_cvt_pk_bf16_f32 v40, v26, v27
	v_cvt_pk_bf16_f32 v41, v28, v29
	global_store_dwordx4 v[36:37], v[38:41], off
	v_pk_mul_f32 v[30:31], v[22:23], s[44:45]
	v_pk_mul_f32 v[32:33], v[24:25], s[44:45]
	v_pk_mul_f32 v[26:27], v[18:19], s[44:45]
	v_pk_mul_f32 v[28:29], v[20:21], s[44:45]
	v_pk_fma_f32 v[30:31], v[22:23], v[30:31], s[46:47] neg_lo:[1,0,0] neg_hi:[1,0,0]
	v_pk_fma_f32 v[32:33], v[24:25], v[32:33], s[46:47] neg_lo:[1,0,0] neg_hi:[1,0,0]
	v_pk_fma_f32 v[26:27], v[18:19], v[26:27], s[46:47] neg_lo:[1,0,0] neg_hi:[1,0,0]
	v_pk_fma_f32 v[28:29], v[20:21], v[28:29], s[46:47] neg_lo:[1,0,0] neg_hi:[1,0,0]
	v_pk_mul_f32 v[30:31], v[22:23], v[30:31]
	v_pk_mul_f32 v[32:33], v[24:25], v[32:33]
	v_pk_mul_f32 v[26:27], v[18:19], v[26:27]
	v_pk_mul_f32 v[28:29], v[20:21], v[28:29]
	v_exp_f32_e32 v30, v30
	v_exp_f32_e32 v31, v31
	v_exp_f32_e32 v32, v32
	v_exp_f32_e32 v33, v33
	v_exp_f32_e32 v26, v26
	v_exp_f32_e32 v27, v27
	v_exp_f32_e32 v28, v28
	v_exp_f32_e32 v29, v29
	v_pk_add_f32 v[30:31], v[30:31], s[48:49]
	v_pk_add_f32 v[32:33], v[32:33], s[48:49]
	v_pk_add_f32 v[26:27], v[26:27], s[48:49]
	v_pk_add_f32 v[28:29], v[28:29], s[48:49]
	v_rcp_f32_e32 v30, v30
	v_rcp_f32_e32 v31, v31
	v_rcp_f32_e32 v32, v32
	v_rcp_f32_e32 v33, v33
	v_rcp_f32_e32 v26, v26
	v_rcp_f32_e32 v27, v27
	v_rcp_f32_e32 v28, v28
	v_rcp_f32_e32 v29, v29
	s_nop 0
	v_pk_mul_f32 v[22:23], v[22:23], v[30:31]
	v_pk_mul_f32 v[24:25], v[24:25], v[32:33]
	v_pk_mul_f32 v[18:19], v[18:19], v[26:27]
	v_pk_mul_f32 v[20:21], v[20:21], v[28:29]
	v_cvt_pk_bf16_f32 v42, v22, v23
	v_cvt_pk_bf16_f32 v43, v24, v25
	v_cvt_pk_bf16_f32 v44, v18, v19
	v_cvt_pk_bf16_f32 v45, v20, v21
	global_store_dwordx4 v[36:37], v[42:45], off offset:256
	s_nop 1
	v_lshlrev_b64 v[18:19], 6, v[0:1]
	v_lshl_add_u64 v[34:35], s[10:11], 0, v[18:19]
	global_load_dwordx4 v[18:21], v[34:35], off
	global_load_dwordx4 v[22:25], v[34:35], off offset:32
	global_load_dwordx4 v[26:29], v[34:35], off offset:16
	global_load_dwordx4 v[30:33], v[34:35], off offset:48
	s_waitcnt vmcnt(3)
	v_mov_b32_e32 v34, v18
	s_waitcnt vmcnt(2)
	v_mov_b32_e32 v35, v22
	v_mov_b32_e32 v22, v19
	v_pk_add_f32 v[18:19], v[34:35], v[22:23]
	v_mov_b32_e32 v22, v20
	v_mov_b32_e32 v23, v24
	v_mov_b32_e32 v24, v21
	v_pk_add_f32 v[20:21], v[22:23], v[24:25]
	s_waitcnt vmcnt(1)
	v_mov_b32_e32 v22, v28
	v_pk_add_f32 v[18:19], v[18:19], v[20:21]
	v_mov_b32_e32 v20, v26
	s_waitcnt vmcnt(0)
	v_mov_b32_e32 v21, v30
	v_mov_b32_e32 v30, v27
	v_mov_b32_e32 v23, v32
	v_mov_b32_e32 v32, v29
	v_pk_add_f32 v[20:21], v[20:21], v[30:31]
	v_pk_add_f32 v[22:23], v[22:23], v[32:33]
	s_nop 0
	v_pk_add_f32 v[20:21], v[20:21], v[22:23]
	s_nop 0
	v_pk_add_f32 v[18:19], v[18:19], v[20:21]
	s_nop 0
	v_add_f32_e32 v1, v18, v19
	v_fma_f32 v1, s6, v1, v132
	v_rsq_f32_e32 v18, v1
	v_mad_i64_i32 v[0:1], s[2:3], v0, s4, 0
	v_lshl_add_u64 v[0:1], v[0:1], 1, s[8:9]
	v_pk_mul_f32 v[14:15], v[14:15], v[18:19] op_sel_hi:[1,0]
	s_nop 0
	v_mul_f32_e32 v19, 0x3dd2d3e8, v14
	v_fma_f32 v19, -v14, v19, s0
	v_mul_f32_e32 v19, v14, v19
	v_mul_f32_e32 v20, 0x3dd2d3e8, v15
	v_exp_f32_e32 v19, v19
	v_fma_f32 v20, -v15, v20, s0
	v_mul_f32_e32 v20, v15, v20
	v_exp_f32_e32 v22, v20
	v_pk_mul_f32 v[16:17], v[16:17], v[18:19] op_sel_hi:[1,0]
	v_lshl_add_u64 v[20:21], v[0:1], 0, v[130:131]
	v_add_f32_e32 v0, 1.0, v19
	v_mul_f32_e32 v19, 0x3dd2d3e8, v16
	v_add_f32_e32 v1, 1.0, v22
	v_fma_f32 v19, -v16, v19, s0
	v_mul_f32_e32 v22, 0x3dd2d3e8, v17
	v_mul_f32_e32 v19, v16, v19
	v_fma_f32 v22, -v17, v22, s0
	v_exp_f32_e32 v19, v19
	v_mul_f32_e32 v22, v17, v22
	v_exp_f32_e32 v23, v22
	v_rcp_f32_e32 v0, v0
	v_add_f32_e32 v19, 1.0, v19
	v_rcp_f32_e32 v22, v19
	v_add_f32_e32 v19, 1.0, v23
	v_pk_mul_f32 v[10:11], v[10:11], v[18:19] op_sel_hi:[1,0]
	v_rcp_f32_e32 v1, v1
	v_mul_f32_e32 v23, 0x3dd2d3e8, v10
	v_fma_f32 v23, -v10, v23, s0
	v_mul_f32_e32 v23, v10, v23
	v_exp_f32_e32 v24, v23
	v_mul_f32_e32 v23, 0x3dd2d3e8, v11
	v_fma_f32 v23, -v11, v23, s0
	v_mul_f32_e32 v23, v11, v23
	v_exp_f32_e32 v25, v23
	v_rcp_f32_e32 v23, v19
	v_add_f32_e32 v19, 1.0, v24
	v_rcp_f32_e32 v24, v19
	v_add_f32_e32 v19, 1.0, v25
	v_pk_mul_f32 v[12:13], v[12:13], v[18:19] op_sel_hi:[1,0]
	v_pk_mul_f32 v[0:1], v[14:15], v[0:1]
	v_mul_f32_e32 v25, 0x3dd2d3e8, v12
	v_fma_f32 v25, -v12, v25, s0
	v_mul_f32_e32 v25, v12, v25
	v_exp_f32_e32 v26, v25
	v_mul_f32_e32 v25, 0x3dd2d3e8, v13
	v_fma_f32 v25, -v13, v25, s0
	v_mul_f32_e32 v25, v13, v25
	v_exp_f32_e32 v27, v25
	v_rcp_f32_e32 v25, v19
	v_add_f32_e32 v19, 1.0, v26
	v_rcp_f32_e32 v26, v19
	v_add_f32_e32 v19, 1.0, v27
	v_rcp_f32_e32 v27, v19
	v_pk_mul_f32 v[14:15], v[16:17], v[22:23]
	v_pk_mul_f32 v[16:17], v[10:11], v[24:25]
	v_cvt_pk_bf16_f32 v10, v0, v1
	v_pk_mul_f32 v[22:23], v[12:13], v[26:27]
	v_cvt_pk_bf16_f32 v11, v14, v15
	v_cvt_pk_bf16_f32 v12, v16, v17
	v_cvt_pk_bf16_f32 v13, v22, v23
	v_pk_mul_f32 v[0:1], v[6:7], v[18:19] op_sel_hi:[1,0]
	v_pk_mul_f32 v[8:9], v[8:9], v[18:19] op_sel_hi:[1,0]
	v_pk_mul_f32 v[2:3], v[2:3], v[18:19] op_sel_hi:[1,0]
	v_pk_mul_f32 v[4:5], v[4:5], v[18:19] op_sel_hi:[1,0]
	v_mul_f32_e32 v6, 0x3dd2d3e8, v0
	v_mul_f32_e32 v7, 0x3dd2d3e8, v1
	global_store_dwordx4 v[20:21], v[10:13], off
	v_mul_f32_e32 v14, 0x3dd2d3e8, v4
	v_mul_f32_e32 v15, 0x3dd2d3e8, v5
	v_mul_f32_e32 v10, 0x3dd2d3e8, v8
	v_mul_f32_e32 v11, 0x3dd2d3e8, v9
	v_mul_f32_e32 v12, 0x3dd2d3e8, v2
	v_mul_f32_e32 v13, 0x3dd2d3e8, v3
	v_fma_f32 v6, -v0, v6, s0
	v_fma_f32 v7, -v1, v7, s0
	v_fma_f32 v10, -v8, v10, s0
	v_fma_f32 v11, -v9, v11, s0
	v_fma_f32 v12, -v2, v12, s0
	v_fma_f32 v13, -v3, v13, s0
	v_fma_f32 v14, -v4, v14, s0
	v_fma_f32 v15, -v5, v15, s0
	v_mul_f32_e32 v6, v0, v6
	v_mul_f32_e32 v7, v1, v7
	v_mul_f32_e32 v10, v8, v10
	v_mul_f32_e32 v11, v9, v11
	v_mul_f32_e32 v12, v2, v12
	v_mul_f32_e32 v13, v3, v13
	v_mul_f32_e32 v14, v4, v14
	v_mul_f32_e32 v15, v5, v15
	v_exp_f32_e32 v6, v6
	v_exp_f32_e32 v7, v7
	v_exp_f32_e32 v10, v10
	v_exp_f32_e32 v11, v11
	v_exp_f32_e32 v12, v12
	v_exp_f32_e32 v13, v13
	v_exp_f32_e32 v14, v14
	v_exp_f32_e32 v15, v15
	v_add_f32_e32 v6, 1.0, v6
	v_add_f32_e32 v7, 1.0, v7
	v_add_f32_e32 v10, 1.0, v10
	v_add_f32_e32 v11, 1.0, v11
	v_add_f32_e32 v12, 1.0, v12
	v_add_f32_e32 v13, 1.0, v13
	v_add_f32_e32 v14, 1.0, v14
	v_add_f32_e32 v15, 1.0, v15
	v_rcp_f32_e32 v6, v6
	v_rcp_f32_e32 v7, v7
	v_rcp_f32_e32 v10, v10
	v_rcp_f32_e32 v11, v11
	v_rcp_f32_e32 v12, v12
	v_rcp_f32_e32 v13, v13
	v_rcp_f32_e32 v14, v14
	v_rcp_f32_e32 v15, v15
	v_pk_mul_f32 v[0:1], v[0:1], v[6:7]
	v_pk_mul_f32 v[6:7], v[8:9], v[10:11]
	v_pk_mul_f32 v[2:3], v[2:3], v[12:13]
	v_pk_mul_f32 v[4:5], v[4:5], v[14:15]
	v_cvt_pk_bf16_f32 v0, v0, v1
	v_cvt_pk_bf16_f32 v1, v6, v7
	v_cvt_pk_bf16_f32 v2, v2, v3
	v_cvt_pk_bf16_f32 v3, v4, v5
	global_store_dwordx4 v[20:21], v[0:3], off offset:256
	s_endpgm
	.p2align	8

	.amdhsa_kernel _Z8gemm_bigIN3pg85EpiUPEEvNS0_4GemmET_
		.amdhsa_group_segment_fixed_size 0
		.amdhsa_private_segment_fixed_size 0
		.amdhsa_kernarg_size 64
		.amdhsa_user_sgpr_count 2
		.amdhsa_user_sgpr_dispatch_ptr 0
		.amdhsa_user_sgpr_queue_ptr 0
		.amdhsa_user_sgpr_kernarg_segment_ptr 1
		.amdhsa_user_sgpr_dispatch_id 0
		.amdhsa_user_sgpr_kernarg_preload_length 0
		.amdhsa_user_sgpr_kernarg_preload_offset 0
		.amdhsa_user_sgpr_private_segment_size 0
		.amdhsa_uses_dynamic_stack 0
		.amdhsa_enable_private_segment 0
		.amdhsa_system_sgpr_workgroup_id_x 1
		.amdhsa_system_sgpr_workgroup_id_y 0
		.amdhsa_system_sgpr_workgroup_id_z 0
		.amdhsa_system_sgpr_workgroup_info 0
		.amdhsa_system_vgpr_workitem_id 0
		.amdhsa_next_free_vgpr 226
		.amdhsa_next_free_sgpr 50
		.amdhsa_accum_offset 228
		.amdhsa_reserve_vcc 0
		.amdhsa_float_round_mode_32 0
		.amdhsa_float_round_mode_16_64 0
		.amdhsa_float_denorm_mode_32 3
		.amdhsa_float_denorm_mode_16_64 3
		.amdhsa_dx10_clamp 1
		.amdhsa_ieee_mode 1
		.amdhsa_fp16_overflow 0
		.amdhsa_tg_split 0
		.amdhsa_exception_fp_ieee_invalid_op 0
		.amdhsa_exception_fp_denorm_src 0
		.amdhsa_exception_fp_ieee_div_zero 0
		.amdhsa_exception_fp_ieee_overflow 0
		.amdhsa_exception_fp_ieee_underflow 0
		.amdhsa_exception_fp_ieee_inexact 0
		.amdhsa_exception_int_div_zero 0
	.end_amdhsa_kernel

.Lfunc_end6:
	.size	_Z8gemm_bigIN3pg85EpiUPEEvNS0_4GemmET_, .Lfunc_end6-_Z8gemm_bigIN3pg85EpiUPEEvNS0_4GemmET_
	.set _Z8gemm_bigIN3pg85EpiUPEEvNS0_4GemmET_.num_vgpr, 226
	.set _Z8gemm_bigIN3pg85EpiUPEEvNS0_4GemmET_.num_agpr, 0
	.set _Z8gemm_bigIN3pg85EpiUPEEvNS0_4GemmET_.numbered_sgpr, 50
	.set _Z8gemm_bigIN3pg85EpiUPEEvNS0_4GemmET_.num_named_barrier, 0
	.set _Z8gemm_bigIN3pg85EpiUPEEvNS0_4GemmET_.private_seg_size, 0
	.set _Z8gemm_bigIN3pg85EpiUPEEvNS0_4GemmET_.uses_vcc, 0
	.set _Z8gemm_bigIN3pg85EpiUPEEvNS0_4GemmET_.uses_flat_scratch, 0
	.set _Z8gemm_bigIN3pg85EpiUPEEvNS0_4GemmET_.has_dyn_sized_stack, 0
	.set _Z8gemm_bigIN3pg85EpiUPEEvNS0_4GemmET_.has_recursion, 0
	.set _Z8gemm_bigIN3pg85EpiUPEEvNS0_4GemmET_.has_indirect_call, 0

amdhsa.kernels:
  - .agpr_count:     0
    .args:
      - .offset:         0
        .size:           136
        .value_kind:     by_value
      - .offset:         136
        .size:           4
        .value_kind:     hidden_block_count_x
      - .offset:         140
        .size:           4
        .value_kind:     hidden_block_count_y
      - .offset:         144
        .size:           4
        .value_kind:     hidden_block_count_z
      - .offset:         148
        .size:           2
        .value_kind:     hidden_group_size_x
      - .offset:         150
        .size:           2
        .value_kind:     hidden_group_size_y
      - .offset:         152
        .size:           2
        .value_kind:     hidden_group_size_z
      - .offset:         154
        .size:           2
        .value_kind:     hidden_remainder_x
      - .offset:         156
        .size:           2
        .value_kind:     hidden_remainder_y
      - .offset:         158
        .size:           2
        .value_kind:     hidden_remainder_z
      - .offset:         176
        .size:           8
        .value_kind:     hidden_global_offset_x
      - .offset:         184
        .size:           8
        .value_kind:     hidden_global_offset_y
      - .offset:         192
        .size:           8
        .value_kind:     hidden_global_offset_z
      - .offset:         200
        .size:           2
        .value_kind:     hidden_grid_dims
    .group_segment_fixed_size: 16640
    .kernarg_segment_align: 8
    .kernarg_segment_size: 392
    .language:       OpenCL C
    .language_version:
      - 2
      - 0
    .max_flat_workgroup_size: 256
    .name:           _Z11prep_kernel8PrepArgs
    .private_segment_fixed_size: 0
    .sgpr_count:     26
    .sgpr_spill_count: 0
    .symbol:         _Z11prep_kernel8PrepArgs.kd
    .uniform_work_group_size: 1
    .uses_dynamic_stack: false
    .vgpr_count:     46
    .vgpr_spill_count: 0
    .wavefront_size: 64
  - .agpr_count:     0
    .args:
      - .offset:         0
        .size:           216
        .value_kind:     by_value
    .group_segment_fixed_size: 0
    .kernarg_segment_align: 8
    .kernarg_segment_size: 216
    .language:       OpenCL C
    .language_version:
      - 2
      - 0
    .max_flat_workgroup_size: 512
    .name:           _Z11attn_kernel8AttnArgs
    .private_segment_fixed_size: 0
    .sgpr_count:     82
    .sgpr_spill_count: 0
    .symbol:         _Z11attn_kernel8AttnArgs.kd
    .uniform_work_group_size: 1
    .uses_dynamic_stack: false
    .vgpr_count:     220
    .vgpr_spill_count: 0
    .wavefront_size: 64
  - .agpr_count:     0
    .args:
      - .offset:         0
        .size:           80
        .value_kind:     by_value
    .group_segment_fixed_size: 98304
    .kernarg_segment_align: 8
    .kernarg_segment_size: 80
    .language:       OpenCL C
    .language_version:
      - 2
      - 0
    .max_flat_workgroup_size: 256
    .name:           _Z7gemm128ILi1ELi96EEv8GemmArgs
    .private_segment_fixed_size: 0
    .sgpr_count:     37
    .sgpr_spill_count: 0
    .symbol:         _Z7gemm128ILi1ELi96EEv8GemmArgs.kd
    .uniform_work_group_size: 1
    .uses_dynamic_stack: false
    .vgpr_count:     256
    .vgpr_spill_count: 0
    .wavefront_size: 64
  - .agpr_count:     0
    .args:
      - .offset:         0
        .size:           80
        .value_kind:     by_value
    .group_segment_fixed_size: 81920
    .kernarg_segment_align: 8
    .kernarg_segment_size: 80
    .language:       OpenCL C
    .language_version:
      - 2
      - 0
    .max_flat_workgroup_size: 256
    .name:           _Z7gemm128ILi2ELi128EEv8GemmArgs
    .private_segment_fixed_size: 0
    .sgpr_count:     38
    .sgpr_spill_count: 0
    .symbol:         _Z7gemm128ILi2ELi128EEv8GemmArgs.kd
    .uniform_work_group_size: 1
    .uses_dynamic_stack: false
    .vgpr_count:     256
    .vgpr_spill_count: 0
    .wavefront_size: 64
  - .agpr_count:     0
    .args:
      - .offset:         0
        .size:           80
        .value_kind:     by_value
    .group_segment_fixed_size: 98304
    .kernarg_segment_align: 8
    .kernarg_segment_size: 80
    .language:       OpenCL C
    .language_version:
      - 2
      - 0
    .max_flat_workgroup_size: 256
    .name:           _Z7gemm128ILi3ELi96EEv8GemmArgs
    .private_segment_fixed_size: 0
    .sgpr_count:     30
    .sgpr_spill_count: 0
    .symbol:         _Z7gemm128ILi3ELi96EEv8GemmArgs.kd
    .uniform_work_group_size: 1
    .uses_dynamic_stack: false
    .vgpr_count:     256
    .vgpr_spill_count: 0
    .wavefront_size: 64
  - .agpr_count:     0
    .args:
      - .offset:         0
        .size:           32
        .value_kind:     by_value
      - .offset:         32
        .size:           56
        .value_kind:     by_value
    .group_segment_fixed_size: 0
    .kernarg_segment_align: 8
    .kernarg_segment_size: 88
    .language:       OpenCL C
    .language_version:
      - 2
      - 0
    .max_flat_workgroup_size: 512
    .name:           _Z8gemm_bigIN3pg86EpiQKVEEvNS0_4GemmET_
    .private_segment_fixed_size: 0
    .sgpr_count:     58
    .sgpr_spill_count: 0
    .symbol:         _Z8gemm_bigIN3pg86EpiQKVEEvNS0_4GemmET_.kd
    .uniform_work_group_size: 1
    .uses_dynamic_stack: false
    .vgpr_count:     228
    .vgpr_spill_count: 0
    .wavefront_size: 64
  - .agpr_count:     0
    .args:
      - .offset:         0
        .size:           32
        .value_kind:     by_value
      - .offset:         32
        .size:           32
        .value_kind:     by_value
    .group_segment_fixed_size: 0
    .kernarg_segment_align: 8
    .kernarg_segment_size: 64
    .language:       OpenCL C
    .language_version:
      - 2
      - 0
    .max_flat_workgroup_size: 512
    .name:           _Z8gemm_bigIN3pg85EpiUPEEvNS0_4GemmET_
    .private_segment_fixed_size: 0
    .sgpr_count:     56
    .sgpr_spill_count: 0
    .symbol:         _Z8gemm_bigIN3pg85EpiUPEEvNS0_4GemmET_.kd
    .uniform_work_group_size: 1
    .uses_dynamic_stack: false
    .vgpr_count:     226
    .vgpr_spill_count: 0
    .wavefront_size: 64
